# v5
# speedup vs baseline: 1.0060x; 1.0060x over previous
_Z12pool3_kernelPKfS0_Pf:
	s_load_dwordx4 s[4:7], s[0:1], 0x0
	s_load_dwordx2 s[8:9], s[0:1], 0x10
	v_and_b32_e32 v1, 63, v0
	v_lshrrev_b32_e32 v2, 6, v0
	v_lshlrev_b32_e32 v3, 5, v1
	v_lshlrev_b32_e32 v4, 4, v1
	s_lshl_b32 s12, s2, 14
	s_lshl_b32 s13, s2, 6
	v_lshl_add_u32 v5, v2, 12, v4
	v_add_u32_e32 v5, s12, v5
	v_lshlrev_b32_e32 v6, 9, v1
	v_lshl_add_u32 v6, v2, 4, v6
	v_add_u32_e32 v6, s13, v6
	v_add_u32_e32 v7, 0x8000, v6
	v_lshlrev_b32_e32 v8, 2, v1
	s_waitcnt lgkmcnt(0)
	s_add_u32 s10, s4, 0x20000
	s_addc_u32 s11, s5, 0
	global_load_dwordx4 v[10:13], v3, s[10:11]
	global_load_dwordx4 v[14:17], v3, s[10:11] offset:16
	global_load_dwordx4 v[20:23], v5, s[4:5]
	global_load_dwordx4 v[24:27], v5, s[4:5] offset:1024
	global_load_dwordx4 v[28:31], v5, s[4:5] offset:2048
	global_load_dwordx4 v[32:35], v5, s[4:5] offset:3072
	global_load_dwordx4 v[36:39], v6, s[6:7]
	global_load_dwordx4 v[40:43], v7, s[6:7]
	s_waitcnt vmcnt(6)
	v_max_f32_e32 v44, v10, v12
	v_max_f32_e32 v45, v14, v16
	v_max_f32_e32 v44, v44, v45
	s_nop 1
	v_max_f32_dpp v44, v44, v44 row_shr:1 row_mask:0xf bank_mask:0xf
	s_nop 1
	v_max_f32_dpp v44, v44, v44 row_shr:2 row_mask:0xf bank_mask:0xf
	s_nop 1
	v_max_f32_dpp v44, v44, v44 row_shr:4 row_mask:0xf bank_mask:0xf
	s_nop 1
	v_max_f32_dpp v44, v44, v44 row_shr:8 row_mask:0xf bank_mask:0xf
	s_nop 1
	v_max_f32_dpp v44, v44, v44 row_bcast:15 row_mask:0xa bank_mask:0xf
	s_nop 1
	v_max_f32_dpp v44, v44, v44 row_bcast:31 row_mask:0xc bank_mask:0xf
	s_nop 1
	v_readlane_b32 s14, v44, 63
	s_nop 1
	v_subrev_f32_e32 v46, s14, v10
	v_subrev_f32_e32 v47, s14, v12
	v_subrev_f32_e32 v48, s14, v14
	v_subrev_f32_e32 v49, s14, v16
	v_mul_f32_e32 v46, 0x3fb8aa3b, v46
	v_mul_f32_e32 v47, 0x3fb8aa3b, v47
	v_mul_f32_e32 v48, 0x3fb8aa3b, v48
	v_mul_f32_e32 v49, 0x3fb8aa3b, v49
	v_exp_f32_e32 v46, v46
	v_exp_f32_e32 v47, v47
	v_exp_f32_e32 v48, v48
	v_exp_f32_e32 v49, v49
	s_nop 0
	v_mul_f32_e32 v50, v11, v46
	v_fmac_f32_e32 v50, v13, v47
	v_fmac_f32_e32 v50, v15, v48
	v_fmac_f32_e32 v50, v17, v49
	s_waitcnt vmcnt(2)
	v_mul_f32_e32 v52, v46, v20
	v_mul_f32_e32 v53, v46, v24
	v_mul_f32_e32 v54, v46, v28
	v_mul_f32_e32 v55, v46, v32
	v_fmac_f32_e32 v52, v47, v21
	v_fmac_f32_e32 v53, v47, v25
	v_fmac_f32_e32 v54, v47, v29
	v_fmac_f32_e32 v55, v47, v33
	v_fmac_f32_e32 v52, v48, v22
	v_fmac_f32_e32 v53, v48, v26
	v_fmac_f32_e32 v54, v48, v30
	v_fmac_f32_e32 v55, v48, v34
	v_fmac_f32_e32 v52, v49, v23
	v_fmac_f32_e32 v53, v49, v27
	v_fmac_f32_e32 v54, v49, v31
	v_fmac_f32_e32 v55, v49, v35
	v_add_f32_dpp v50, v50, v50 row_shr:1 row_mask:0xf bank_mask:0xf
	v_add_f32_dpp v52, v52, v52 row_shr:1 row_mask:0xf bank_mask:0xf
	v_add_f32_dpp v53, v53, v53 row_shr:1 row_mask:0xf bank_mask:0xf
	v_add_f32_dpp v54, v54, v54 row_shr:1 row_mask:0xf bank_mask:0xf
	v_add_f32_dpp v55, v55, v55 row_shr:1 row_mask:0xf bank_mask:0xf
	v_add_f32_dpp v50, v50, v50 row_shr:2 row_mask:0xf bank_mask:0xf
	v_add_f32_dpp v52, v52, v52 row_shr:2 row_mask:0xf bank_mask:0xf
	v_add_f32_dpp v53, v53, v53 row_shr:2 row_mask:0xf bank_mask:0xf
	v_add_f32_dpp v54, v54, v54 row_shr:2 row_mask:0xf bank_mask:0xf
	v_add_f32_dpp v55, v55, v55 row_shr:2 row_mask:0xf bank_mask:0xf
	v_add_f32_dpp v50, v50, v50 row_shr:4 row_mask:0xf bank_mask:0xf
	v_add_f32_dpp v52, v52, v52 row_shr:4 row_mask:0xf bank_mask:0xf
	v_add_f32_dpp v53, v53, v53 row_shr:4 row_mask:0xf bank_mask:0xf
	v_add_f32_dpp v54, v54, v54 row_shr:4 row_mask:0xf bank_mask:0xf
	v_add_f32_dpp v55, v55, v55 row_shr:4 row_mask:0xf bank_mask:0xf
	v_add_f32_dpp v50, v50, v50 row_shr:8 row_mask:0xf bank_mask:0xf
	v_add_f32_dpp v52, v52, v52 row_shr:8 row_mask:0xf bank_mask:0xf
	v_add_f32_dpp v53, v53, v53 row_shr:8 row_mask:0xf bank_mask:0xf
	v_add_f32_dpp v54, v54, v54 row_shr:8 row_mask:0xf bank_mask:0xf
	v_add_f32_dpp v55, v55, v55 row_shr:8 row_mask:0xf bank_mask:0xf
	v_add_f32_dpp v50, v50, v50 row_bcast:15 row_mask:0xa bank_mask:0xf
	v_add_f32_dpp v52, v52, v52 row_bcast:15 row_mask:0xa bank_mask:0xf
	v_add_f32_dpp v53, v53, v53 row_bcast:15 row_mask:0xa bank_mask:0xf
	v_add_f32_dpp v54, v54, v54 row_bcast:15 row_mask:0xa bank_mask:0xf
	v_add_f32_dpp v55, v55, v55 row_bcast:15 row_mask:0xa bank_mask:0xf
	v_add_f32_dpp v50, v50, v50 row_bcast:31 row_mask:0xc bank_mask:0xf
	v_add_f32_dpp v52, v52, v52 row_bcast:31 row_mask:0xc bank_mask:0xf
	v_add_f32_dpp v53, v53, v53 row_bcast:31 row_mask:0xc bank_mask:0xf
	v_add_f32_dpp v54, v54, v54 row_bcast:31 row_mask:0xc bank_mask:0xf
	v_add_f32_dpp v55, v55, v55 row_bcast:31 row_mask:0xc bank_mask:0xf
	s_nop 1
	v_readlane_b32 s15, v50, 63
	v_readlane_b32 s16, v52, 63
	v_readlane_b32 s17, v53, 63
	v_readlane_b32 s18, v54, 63
	v_readlane_b32 s19, v55, 63
	s_nop 1
	v_mov_b32_e32 v56, s15
	v_rcp_f32_e32 v56, v56
	s_nop 0
	v_mul_f32_e32 v57, s16, v56
	v_mul_f32_e32 v58, s17, v56
	v_mul_f32_e32 v59, s18, v56
	v_mul_f32_e32 v60, s19, v56
	s_waitcnt vmcnt(0)
	v_mul_f32_e32 v61, v36, v57
	v_mul_f32_e32 v62, v40, v57
	v_fmac_f32_e32 v61, v37, v58
	v_fmac_f32_e32 v62, v41, v58
	v_fmac_f32_e32 v61, v38, v59
	v_fmac_f32_e32 v62, v42, v59
	v_fmac_f32_e32 v61, v39, v60
	v_fmac_f32_e32 v62, v43, v60
	global_atomic_add_f32 v8, v61, s[8:9]
	global_atomic_add_f32 v8, v62, s[8:9] offset:256
	s_endpgm

	.amdhsa_kernel _Z12pool3_kernelPKfS0_Pf
		.amdhsa_group_segment_fixed_size 18592
		.amdhsa_private_segment_fixed_size 0
		.amdhsa_kernarg_size 24
		.amdhsa_user_sgpr_count 2
		.amdhsa_user_sgpr_dispatch_ptr 0
		.amdhsa_user_sgpr_queue_ptr 0
		.amdhsa_user_sgpr_kernarg_segment_ptr 1
		.amdhsa_user_sgpr_dispatch_id 0
		.amdhsa_user_sgpr_kernarg_preload_length 0
		.amdhsa_user_sgpr_kernarg_preload_offset 0
		.amdhsa_user_sgpr_private_segment_size 0
		.amdhsa_uses_dynamic_stack 0
		.amdhsa_enable_private_segment 0
		.amdhsa_system_sgpr_workgroup_id_x 1
		.amdhsa_system_sgpr_workgroup_id_y 0
		.amdhsa_system_sgpr_workgroup_id_z 0
		.amdhsa_system_sgpr_workgroup_info 0
		.amdhsa_system_vgpr_workitem_id 0
		.amdhsa_next_free_vgpr 64
		.amdhsa_next_free_sgpr 20
		.amdhsa_accum_offset 64
		.amdhsa_reserve_vcc 1
		.amdhsa_float_round_mode_32 0
		.amdhsa_float_round_mode_16_64 0
		.amdhsa_float_denorm_mode_32 3
		.amdhsa_float_denorm_mode_16_64 3
		.amdhsa_dx10_clamp 1
		.amdhsa_ieee_mode 1
		.amdhsa_fp16_overflow 0
		.amdhsa_tg_split 0
		.amdhsa_exception_fp_ieee_invalid_op 0
		.amdhsa_exception_fp_denorm_src 0
		.amdhsa_exception_fp_ieee_div_zero 0
		.amdhsa_exception_fp_ieee_overflow 0
		.amdhsa_exception_fp_ieee_underflow 0
		.amdhsa_exception_fp_ieee_inexact 0
		.amdhsa_exception_int_div_zero 0
	.end_amdhsa_kernel

.Lfunc_end1:
	.size	_Z12pool3_kernelPKfS0_Pf, .Lfunc_end1-_Z12pool3_kernelPKfS0_Pf
	.set _Z12pool3_kernelPKfS0_Pf.num_vgpr, 64
	.set _Z12pool3_kernelPKfS0_Pf.num_agpr, 0
	.set _Z12pool3_kernelPKfS0_Pf.numbered_sgpr, 20
	.set _Z12pool3_kernelPKfS0_Pf.num_named_barrier, 0
	.set _Z12pool3_kernelPKfS0_Pf.private_seg_size, 0
	.set _Z12pool3_kernelPKfS0_Pf.uses_vcc, 1
	.set _Z12pool3_kernelPKfS0_Pf.uses_flat_scratch, 0
	.set _Z12pool3_kernelPKfS0_Pf.has_dyn_sized_stack, 0
	.set _Z12pool3_kernelPKfS0_Pf.has_recursion, 0
	.set _Z12pool3_kernelPKfS0_Pf.has_indirect_call, 0

amdhsa.kernels:
  - .agpr_count:     0
    .args:
      - .actual_access:  read_only
        .address_space:  global
        .offset:         0
        .size:           8
        .value_kind:     global_buffer
      - .actual_access:  read_only
        .address_space:  global
        .offset:         8
        .size:           8
        .value_kind:     global_buffer
      - .actual_access:  read_only
        .address_space:  global
        .offset:         16
        .size:           8
        .value_kind:     global_buffer
      - .actual_access:  read_only
        .address_space:  global
        .offset:         24
        .size:           8
        .value_kind:     global_buffer
      - .actual_access:  read_only
        .address_space:  global
        .offset:         32
        .size:           8
        .value_kind:     global_buffer
      - .actual_access:  read_only
        .address_space:  global
        .offset:         40
        .size:           8
        .value_kind:     global_buffer
      - .actual_access:  read_only
        .address_space:  global
        .offset:         48
        .size:           8
        .value_kind:     global_buffer
      - .actual_access:  read_only
        .address_space:  global
        .offset:         56
        .size:           8
        .value_kind:     global_buffer
      - .actual_access:  read_only
        .address_space:  global
        .offset:         64
        .size:           8
        .value_kind:     global_buffer
      - .actual_access:  read_only
        .address_space:  global
        .offset:         72
        .size:           8
        .value_kind:     global_buffer
      - .actual_access:  write_only
        .address_space:  global
        .offset:         80
        .size:           8
        .value_kind:     global_buffer
      - .actual_access:  write_only
        .address_space:  global
        .offset:         88
        .size:           8
        .value_kind:     global_buffer
    .group_segment_fixed_size: 161344
    .kernarg_segment_align: 8
    .kernarg_segment_size: 96
    .language:       OpenCL C
    .language_version:
      - 2
      - 0
    .max_flat_workgroup_size: 512
    .name:           _Z12pool1_kernelPKfS0_S0_S0_S0_S0_S0_S0_S0_S0_PfS1_
    .private_segment_fixed_size: 0
    .sgpr_count:     42
    .sgpr_spill_count: 0
    .symbol:         _Z12pool1_kernelPKfS0_S0_S0_S0_S0_S0_S0_S0_S0_PfS1_.kd
    .uniform_work_group_size: 1
    .uses_dynamic_stack: false
    .vgpr_count:     256
    .vgpr_spill_count: 0
    .wavefront_size: 64
  - .agpr_count:     0
    .args:
      - .actual_access:  read_only
        .address_space:  global
        .offset:         0
        .size:           8
        .value_kind:     global_buffer
      - .actual_access:  read_only
        .address_space:  global
        .offset:         8
        .size:           8
        .value_kind:     global_buffer
      - .address_space:  global
        .offset:         16
        .size:           8
        .value_kind:     global_buffer
    .group_segment_fixed_size: 18592
    .kernarg_segment_align: 8
    .kernarg_segment_size: 24
    .language:       OpenCL C
    .language_version:
      - 2
      - 0
    .max_flat_workgroup_size: 256
    .name:           _Z12pool3_kernelPKfS0_Pf
    .private_segment_fixed_size: 0
    .sgpr_count:     26
    .sgpr_spill_count: 0
    .symbol:         _Z12pool3_kernelPKfS0_Pf.kd
    .uniform_work_group_size: 1
    .uses_dynamic_stack: false
    .vgpr_count:     64
    .vgpr_spill_count: 0
    .wavefront_size: 64
